# conversion slot per CU = (vcu>>4)%12 so concurrently converting CUs are consecutive (spread over weight columns)
# speedup vs baseline: 1.0026x; 1.0026x over previous
.LBB0_238:
	s_add_u32 s10, s42, s0
	s_addc_u32 s11, s43, s1
	global_load_dwordx4 v[6:9], v5, s[10:11] offset:16
	global_load_dwordx4 v[10:13], v5, s[10:11]
	s_add_u32 s10, s44, s0
	s_addc_u32 s11, s45, s1
	global_load_dwordx4 v[14:17], v5, s[10:11]
	global_load_dwordx4 v[18:21], v5, s[10:11] offset:16
	s_add_u32 s0, s0, 32
	s_addc_u32 s1, s1, 0
	s_cmpk_eq_i32 s0, 0x100
	s_waitcnt vmcnt(2)
	v_max3_f32 v0, v2, |v10|, |v11|
	v_max3_f32 v0, v0, |v12|, |v13|
	s_waitcnt vmcnt(1)
	v_max3_f32 v2, v4, |v14|, |v15|
	v_max3_f32 v0, v0, |v6|, |v7|
	v_max3_f32 v4, v2, |v16|, |v17|
	v_max3_f32 v2, v0, |v8|, |v9|
	s_waitcnt vmcnt(0)
	v_max3_f32 v0, v4, |v18|, |v19|
	v_max3_f32 v4, v0, |v20|, |v21|
	s_cbranch_scc0 .LBB0_238
	v_mov_b32_e32 v0, 0x10000
	global_load_dword v5, v0, s[34:35] offset:256 sc1
	s_movk_i32 s10, 0x180
	s_and_b64 s[0:1], s[86:87], exec
	s_cselect_b32 s97, s10, 0xc00
	s_add_i32 s14, s95, s97
	s_cmpk_lt_i32 s94, 0x1800
	s_cselect_b64 s[60:61], -1, 0
	s_add_i32 s0, s94, 0xfffff000
	s_lshr_b32 s42, s0, 6
	s_mov_b32 s43, 0
	s_lshl_b64 s[0:1], s[42:43], 22
	s_lshl_b64 s[10:11], s[42:43], 24
	s_add_u32 s58, s24, s10
	s_addc_u32 s59, s25, s11
	s_lshr_b32 s10, s6, 25
	s_add_i32 s11, s94, s10
	s_ashr_i32 s10, s11, 7
	s_and_b32 s11, s11, 0xff80
	s_sub_i32 s44, s94, s11
	s_bfe_i32 s45, s44, 0x80000
	s_bfe_u32 s45, s45, 0x4000b
	s_add_i32 s45, s44, s45
	s_bfe_i32 s52, s45, 0x80000
	s_and_b32 s45, s45, 0xf0
	s_sub_i32 s44, s44, s45
	s_sext_i32_i8 s44, s44
	s_lshl_b32 s62, s44, 8
	s_mul_i32 s44, s9, s4
	s_ashr_i32 s11, s10, 31
	v_readlane_b32 s54, v254, 9
	s_sub_i32 s44, s7, s44
	s_lshl_b32 s15, s94, 5
	s_lshl_b32 s42, s94, 8
	s_lshl_b64 s[12:13], s[10:11], 25
	s_lshl_b64 s[10:11], s[10:11], 23
	s_lshl_b32 s55, s54, 1
	s_xor_b32 s8, s6, s8
	s_add_i32 s45, s9, 1
	s_sub_i32 s53, s44, s4
	s_cmp_ge_u32 s44, s4
	s_cselect_b32 s9, s45, s9
	s_cselect_b32 s44, s53, s44
	s_add_i32 s45, s9, 1
	s_cmp_ge_u32 s44, s4
	s_cselect_b32 s9, s45, s9
	s_xor_b32 s9, s9, s8
	s_sub_i32 s82, s9, s8
	s_add_i32 s8, s14, -1
	s_cmpk_lt_i32 s94, 0x1000
	s_cselect_b64 s[56:57], -1, 0
	s_add_u32 s45, s16, s0
	s_addc_u32 s53, s17, s1
	s_and_b32 s44, s15, 0x700
	s_and_b32 s64, s42, 0x700
	s_add_u32 s42, s20, s12
	s_addc_u32 s15, s21, s13
	v_mul_f32_e32 v0, 0x4f7ffffe, v3
	s_sext_i32_i16 s52, s52
	s_add_u32 s63, s40, s10
	v_cvt_u32_f32_e32 v0, v0
	s_addc_u32 s11, s41, s11
	s_lshl_b32 s0, s52, 4
	s_and_b32 s52, s0, 0xffffff00
	v_writelane_b32 v254, s55, 17
	s_or_b32 s0, s55, 1
	v_writelane_b32 v254, s0, 21
	s_mul_i32 s0, s82, s95
	s_sub_i32 s1, 1, s14
	s_sub_i32 s80, s94, s0
	s_xor_b32 s0, s8, s95
	s_max_i32 s1, s8, s1
	v_readfirstlane_b32 s8, v0
	s_mul_i32 s5, s5, s8
	s_mul_hi_u32 s5, s8, s5
	s_add_i32 s8, s8, s5
	s_mul_hi_u32 s5, s1, s8
	s_mul_i32 s8, s5, s4
	s_sub_i32 s1, s1, s8
	s_lshl_b32 s69, s54, 5
	s_ashr_i32 s0, s0, 31
	s_add_i32 s8, s5, 1
	s_sub_i32 s9, s1, s4
	s_cmp_ge_u32 s1, s4
	s_cselect_b32 s5, s8, s5
	s_cselect_b32 s1, s9, s1
	s_add_i32 s8, s5, 1
	s_cmp_ge_u32 s1, s4
	s_cselect_b32 s1, s8, s5
	s_xor_b32 s1, s1, s0
	s_sub_i32 s0, s1, s0
	s_abs_i32 s8, s0
	v_cvt_f32_u32_e32 v0, s8
	v_writelane_b32 v254, s60, 15
	s_mov_b64 s[86:87], -1
	s_cmp_ge_i32 s80, s97
	v_rcp_iflag_f32_e32 v0, v0
	v_writelane_b32 v254, s61, 16
	v_cndmask_b32_e64 v199, 0, 1, s[60:61]
	v_mul_f32_e32 v0, 0x4f7ffffe, v0
	v_cvt_u32_f32_e32 v0, v0
	s_nop 0
	v_readfirstlane_b32 s0, v0
	s_cbranch_scc1 .LBB0_355
	s_sub_i32 s1, 0, s8
	s_mul_i32 s1, s1, s0
	s_mul_hi_u32 s1, s0, s1
	s_add_i32 s0, s0, s1
	v_mul_f32_e32 v2, 0x4138aa3b, v2
	s_mul_hi_u32 s9, s7, s0
	v_mul_f32_e32 v2, v4, v2
	s_mov_b32 s0, 0x41600000
	s_waitcnt vmcnt(0)
	v_lshlrev_b32_e32 v4, 16, v5
	v_cmp_nge_f32_e32 vcc, s0, v2
	s_mov_b32 s0, 0x476a6000
	s_mul_i32 s9, s9, s8
	v_cmp_ngt_f32_e64 s[0:1], s0, v4
	s_sub_i32 s7, s7, s9
	s_or_b64 s[0:1], vcc, s[0:1]
	s_sub_i32 s9, s7, s8
	s_cmp_ge_u32 s7, s8
	s_cselect_b32 s7, s9, s7
	s_sub_i32 s9, s7, s8
	s_cmp_ge_u32 s7, s8
	s_cselect_b32 s7, s9, s7
	s_xor_b32 s7, s7, s6
	s_sub_i32 s81, s7, s6
	s_lshr_b32 s81, s94, 4
	s_add_i32 s7, s81, -12
	s_cmp_ge_u32 s81, 12
	s_cselect_b32 s81, s7, s81
	s_cmp_lg_u32 0, -1
	v_and_b32_e32 v0, 63, v235
	v_lshlrev_b32_e32 v2, 1, v235
	s_cselect_b32 s6, 0, 0
	v_cmp_gt_u32_e64 s[4:5], 32, v0
	v_mul_u32_u24_e32 v208, 0x300, v0
	v_lshlrev_b32_e32 v0, 3, v235
	v_and_b32_e32 v2, 32, v2
	s_add_i32 s7, s6, 0x12000
	v_and_b32_e32 v209, 24, v0
	v_and_b32_e32 v200, 56, v0
	v_add_u32_e32 v0, s7, v2
	s_add_u32 s7, s34, 0xc5600000
	v_writelane_b32 v254, s7, 20
	s_addc_u32 s7, s35, 0
	v_writelane_b32 v254, s7, 19
	v_writelane_b32 v254, s62, 22
	v_writelane_b32 v254, s64, 23
	s_add_u32 s12, s34, 0x5b600000
	v_writelane_b32 v254, s44, 24
	v_lshlrev_b32_e32 v4, 4, v235
	s_addc_u32 s13, s35, 0
	v_writelane_b32 v254, s52, 25
	v_bfe_u32 v6, v235, 5, 1
	v_and_b32_e32 v4, 0xc0, v4
	s_add_u32 s8, s34, 0x5ce00000
	v_writelane_b32 v254, s53, 26
	v_lshl_or_b32 v4, v6, 8, v4
	s_addc_u32 s9, s35, 0
	s_add_i32 s6, s6, 0xc000
	v_writelane_b32 v254, s11, 27
	s_movk_i32 s10, 0x800
	v_add3_u32 v214, v0, v209, v4
	v_add3_u32 v0, v2, s6, v209
	s_and_b64 s[6:7], s[56:57], exec
	v_writelane_b32 v254, s45, 28
	s_cselect_b32 s14, 0x1000, s10
	s_cselect_b32 s11, s11, s53
	v_writelane_b32 v254, s63, 29
	s_cselect_b32 s10, s63, s45
	v_writelane_b32 v254, s10, 30
	s_cselect_b32 s6, s52, s44
	s_cselect_b32 s54, s62, s64
	v_writelane_b32 v254, s11, 31
	v_writelane_b32 v254, s59, 32
	v_writelane_b32 v254, s15, 33
	v_writelane_b32 v254, s58, 34
	v_writelane_b32 v254, s42, 35
	s_cselect_b32 s15, s15, s59
	s_cselect_b32 s42, s42, s58
	v_writelane_b32 v254, s6, 36
	s_add_i32 s6, s6, s69
	s_ashr_i32 s7, s6, 31
	s_and_b64 s[10:11], s[56:57], exec
	s_cselect_b32 s10, 12, 11
	s_lshl_b64 s[6:7], s[6:7], s10
	s_lshl_b64 s[6:7], s[6:7], 2
	s_add_u32 s10, s42, s6
	s_mov_b32 s6, s54
	s_addc_u32 s11, s15, s7
	s_ashr_i32 s55, s54, 31
	v_writelane_b32 v254, s6, 37
	v_cndmask_b32_e64 v215, 0, 1, s[56:57]
	s_mov_b32 s45, s43
	v_writelane_b32 v254, s7, 38
	s_lshl_b64 s[6:7], s[54:55], 2
	s_add_u32 s6, s10, s6
	s_addc_u32 s7, s11, s7
	v_writelane_b32 v254, s6, 39
	s_mov_b32 s10, 0x7c000
	s_mov_b32 s11, 0x1e000
	v_writelane_b32 v254, s7, 40
	s_and_b64 s[6:7], s[56:57], exec
	s_cselect_b32 s6, s10, 0x3e000
	s_mov_b32 s7, s43
	v_writelane_b32 v254, s6, 41
	s_mov_b32 s10, 0x24000
	v_bfe_u32 v3, v235, 3, 3
	v_writelane_b32 v254, s7, 42
	s_mov_b32 s6, 0x78000
	s_cselect_b32 s6, s6, 0x3c000
	s_mov_b32 s7, s43
	v_writelane_b32 v254, s6, 43
	v_and_b32_e32 v207, 31, v235
	v_add_u32_e32 v8, 0, v2
	v_writelane_b32 v254, s7, 44
	s_mov_b32 s6, 0x74000
	s_cselect_b32 s6, s6, 0x3a000
	s_mov_b32 s7, s43
	v_writelane_b32 v254, s6, 45
	v_lshlrev_b32_e32 v203, 7, v3
	v_lshlrev_b32_e32 v5, 10, v6
	v_writelane_b32 v254, s7, 46
	s_mov_b32 s6, 0x70000
	s_cselect_b32 s6, s6, 0x38000
	s_mov_b32 s7, s43
	v_writelane_b32 v254, s6, 47
	v_lshlrev_b32_e32 v7, 4, v207
	v_mul_u32_u24_e32 v9, 0x600, v207
	v_writelane_b32 v254, s7, 48
	s_mov_b32 s6, 0x6c000
	s_cselect_b32 s6, s6, 0x36000
	s_mov_b32 s7, s43
	v_writelane_b32 v254, s6, 49
	v_add3_u32 v211, v8, v209, v4
	v_mul_u32_u24_e32 v196, 0x600, v3
	v_writelane_b32 v254, s7, 50
	s_mov_b32 s6, 0x68000
	s_cselect_b32 s6, s6, 0x34000
	s_mov_b32 s7, s43
	v_writelane_b32 v254, s6, 51
	v_bfe_u32 v201, v235, 2, 4
	v_lshlrev_b32_e32 v202, 9, v6
	v_writelane_b32 v254, s7, 52
	s_mov_b32 s6, 0x64000
	s_cselect_b32 s6, s6, 0x32000
	s_mov_b32 s7, s43
	v_writelane_b32 v254, s6, 53
	v_mov_b32_e32 v3, 0
	v_or_b32_e32 v204, 0x400, v203
	v_writelane_b32 v254, s7, 54
	s_mov_b32 s6, 0x60000
	s_cselect_b32 s6, s6, 0x30000
	s_mov_b32 s7, s43
	v_writelane_b32 v254, s6, 55
	v_or_b32_e32 v205, 0x800, v203
	v_or_b32_e32 v206, 0xc00, v203
	v_writelane_b32 v254, s7, 56
	s_mov_b32 s6, 0x5c000
	s_cselect_b32 s6, s6, 0x2e000
	s_mov_b32 s7, s43
	v_writelane_b32 v254, s6, 57
	v_lshl_or_b32 v198, v6, 3, v9
	v_add3_u32 v210, 0, v5, v7
	v_writelane_b32 v254, s7, 58
	s_mov_b32 s6, 0x58000
	s_cselect_b32 s6, s6, 0x2c000
	s_mov_b32 s7, s43
	v_writelane_b32 v254, s6, 59
	v_add_u32_e32 v212, 0xc000, v211
	v_lshlrev_b32_e32 v213, 4, v6
	v_writelane_b32 v254, s7, 60
	s_mov_b32 s6, 0x54000
	s_cselect_b32 s6, s6, 0x2a000
	s_mov_b32 s7, s43
	v_writelane_b32 v254, s6, 61
	s_mul_i32 s82, s82, s97
	s_mov_b32 s52, -4.0
	v_writelane_b32 v254, s7, 62
	s_mov_b32 s6, 0x50000
	s_cselect_b32 s6, s6, 0x28000
	s_mov_b32 s7, s43
	v_writelane_b32 v254, s6, 63
	s_mov_b32 s83, 0
	s_nop 0
	v_writelane_b32 v255, s7, 0
	s_mov_b32 s6, 0x4c000
	s_cselect_b32 s6, s6, 0x26000
	s_mov_b32 s7, s43
	v_writelane_b32 v255, s6, 1
	s_nop 1
	v_writelane_b32 v255, s7, 2
	s_mov_b32 s6, 0x48000
	s_cselect_b32 s6, s6, 0x24000
	s_mov_b32 s7, s43
	v_writelane_b32 v255, s6, 3
	s_nop 1
	v_writelane_b32 v255, s7, 4
	s_mov_b32 s6, 0x44000
	s_cselect_b32 s6, s6, 0x22000
	s_mov_b32 s7, s43
	v_writelane_b32 v255, s6, 5
	s_nop 1
	v_writelane_b32 v255, s7, 6
	s_lshl_b32 s6, s14, 6
	s_mov_b32 s7, s43
	v_writelane_b32 v255, s6, 7
	s_nop 1
	v_writelane_b32 v255, s7, 8
	v_writelane_b32 v255, s56, 9
	s_and_b64 s[6:7], s[56:57], exec
	s_cselect_b32 s6, 0x3c000, s11
	v_writelane_b32 v255, s57, 10
	s_mov_b32 s7, s43
	v_writelane_b32 v255, s6, 11
	s_cselect_b32 s10, s10, 0x12000
	s_mov_b32 s11, s43
	v_writelane_b32 v255, s7, 12
	s_mov_b32 s6, 0x1c000
	s_cselect_b32 s6, 0x38000, s6
	s_mov_b32 s7, s43
	v_writelane_b32 v255, s6, 13
	s_nop 1
	v_writelane_b32 v255, s7, 14
	s_mov_b32 s6, 0x1a000
	s_cselect_b32 s6, 0x34000, s6
	s_mov_b32 s7, s43
	v_writelane_b32 v255, s6, 15
	s_nop 1
	v_writelane_b32 v255, s7, 16
	s_mov_b32 s6, 0x18000
	s_cselect_b32 s44, 0x30000, s6
	v_writelane_b32 v255, s44, 17
	s_mov_b32 s7, 0x16000
	s_cselect_b32 s6, s6, 0xc000
	v_writelane_b32 v255, s45, 18
	s_cselect_b32 s44, 0x2c000, s7
	s_mov_b32 s45, s43
	v_writelane_b32 v255, s44, 19
	s_mov_b32 s7, 0x14000
	s_nop 0
	v_writelane_b32 v255, s45, 20
	s_cselect_b32 s44, 0x28000, s7
	s_mov_b32 s45, s43
	v_writelane_b32 v255, s44, 21
	s_mov_b32 s7, 0xe000
	s_nop 0
	v_writelane_b32 v255, s45, 22
	v_writelane_b32 v255, s10, 23
	s_mov_b32 s45, 0x41000000
	s_nop 0
	v_writelane_b32 v255, s11, 24
	s_cselect_b32 s10, 0x1c000, s7
	s_mov_b32 s11, s43
	v_writelane_b32 v255, s10, 25
	s_mov_b32 s7, s43
	s_nop 0
	v_writelane_b32 v255, s11, 26
	v_writelane_b32 v255, s6, 27
	s_mov_b32 s11, s43
	s_nop 0
	v_writelane_b32 v255, s7, 28
	s_mov_b32 s6, 0xa000
	s_cselect_b32 s6, 0x14000, s6
	s_mov_b32 s7, s43
	v_writelane_b32 v255, s6, 29
	s_nop 1
	v_writelane_b32 v255, s7, 30
	s_movk_i32 s6, 0x6000
	s_cselect_b32 s10, 0xc000, s6
	v_writelane_b32 v255, s10, 31
	v_add3_u32 v216, v0, v4, s6
	s_mov_b64 s[6:7], 0
	v_writelane_b32 v255, s11, 32
	s_lshl_b32 s10, s14, 5
	s_sub_u32 s10, 0, s10
	s_subb_u32 s11, 0, 0
	v_writelane_b32 v255, s10, 33
	s_nop 1
	v_writelane_b32 v255, s11, 34
	s_lshl_b32 s10, s14, 4
	s_sub_u32 s10, 0, s10
	s_subb_u32 s11, 0, 0
	v_writelane_b32 v255, s10, 35
	s_nop 1
	v_writelane_b32 v255, s11, 36
	s_lshl_b32 s10, s14, 3
	s_sub_u32 s10, 0, s10
	s_subb_u32 s11, 0, 0
	v_writelane_b32 v255, s10, 37
	s_nop 1
	v_writelane_b32 v255, s11, 38
	s_lshl_b32 s10, s14, 2
	s_sub_u32 s10, 0, s10
	s_subb_u32 s11, 0, 0
	v_writelane_b32 v255, s10, 39
	s_nop 1
	v_writelane_b32 v255, s11, 40
	s_branch .LBB0_243
